# per-phase instruction prefetch: on entry to each phase every workgroup touches its slice of that phase's code (s_getpc base), on top of the kernel-entry code warm
# speedup vs baseline: 1.0117x; 1.0053x over previous
.LBB0_135:
	s_getpc_b64 s[98:99]
	s_and_b32 s98, s98, 0xffffff80
	v_readlane_b32 s97, v252, 2
	s_nop 0
	s_and_b32 s97, s97, 31
	s_mul_i32 s97, s97, 0x100
	s_add_u32 s98, s98, s97
	s_addc_u32 s99, s99, 0
	v_and_b32_e32 v254, 63, v0
	v_min_u32_e32 v254, 1, v254
	v_lshlrev_b32_e32 v254, 7, v254
	global_load_dword v254, v254, s[98:99]
	s_add_u32 s38, s50, 0x1800000
	s_addc_u32 s39, s51, 0
	s_cmp_lt_i32 s88, 2
	s_cselect_b64 s[0:1], -1, 0
	s_cmp_gt_i32 s89, 1
	s_cselect_b64 s[4:5], -1, 0
	s_and_b64 s[0:1], s[0:1], s[4:5]
	s_andn2_b64 vcc, exec, s[0:1]
	s_cbranch_vccnz .LBB0_214
	s_cmpk_gt_i32 s2, 0x3ff
	v_readfirstlane_b32 s5, v0
	s_cbranch_scc1 .LBB0_160
	s_ashr_i32 s36, s2, 31
	s_lshr_b32 s0, s36, 29
	s_add_i32 s10, s2, s0
	s_and_b32 s0, s10, -8
	s_sub_i32 s11, s2, s0
	s_cmp_gt_i32 s11, -1
	s_cbranch_scc0 .LBB0_139
	s_lshl_b32 s4, s11, 7
	s_cbranch_execz .LBB0_140
	s_branch .LBB0_141

.LBB0_214:
	s_getpc_b64 s[98:99]
	s_and_b32 s98, s98, 0xffffff80
	v_readlane_b32 s97, v252, 2
	s_nop 0
	s_and_b32 s97, s97, 31
	s_mul_i32 s97, s97, 0x400
	s_add_u32 s98, s98, s97
	s_addc_u32 s99, s99, 0
	v_and_b32_e32 v254, 63, v0
	v_min_u32_e32 v254, 7, v254
	v_lshlrev_b32_e32 v254, 7, v254
	global_load_dword v254, v254, s[98:99]
	s_cmp_lt_i32 s88, 3
	s_cselect_b64 s[0:1], -1, 0
	s_cmp_gt_i32 s89, 2
	s_cselect_b64 s[4:5], -1, 0
	s_and_b64 s[0:1], s[0:1], s[4:5]
	s_andn2_b64 vcc, exec, s[0:1]
	s_cbranch_vccnz .LBB0_533
	v_mov_b32_e32 v1, v0
	s_cmpk_gt_i32 s2, 0x3ff
	v_readfirstlane_b32 s4, v1
	s_cbranch_scc1 .LBB0_473
	s_movk_i32 s0, 0x80
	v_cmp_gt_i32_e32 vcc, s0, v1
	s_and_saveexec_b64 s[0:1], vcc
	s_add_i32 s5, 0, 0x1b200
	v_lshl_add_u32 v2, v1, 2, s5
	v_mov_b32_e32 v3, 0
	ds_write_b32 v2, v3 offset:1024
	s_or_b64 exec, exec, s[0:1]
	s_ashr_i32 s1, s2, 31
	s_lshr_b32 s0, s1, 25
	s_ashr_i32 s5, s2, 2
	s_lshr_b32 s1, s1, 27
	s_add_i32 s0, s2, s0
	s_add_i32 s1, s5, s1
	s_ashr_i32 s0, s0, 7
	s_andn2_b32 s1, s1, 31
	s_sub_i32 s12, s5, s1
	s_ashr_i32 s1, s0, 31
	s_lshl_b64 s[10:11], s[0:1], 11
	s_lshl_b32 s1, s12, 6
	s_and_b32 s13, s2, 3
	s_ashr_i32 s5, s1, 31
	s_waitcnt lgkmcnt(0)
	s_barrier
	s_add_u32 s10, s10, s1
	s_addc_u32 s11, s11, s5
	s_ashr_i32 s14, s4, 6
	s_cmp_lt_i32 s14, 4
	v_and_b32_e32 v2, 63, v1
	s_cbranch_scc1 .LBB0_224
	s_cmp_eq_u32 s14, 4
	s_mov_b64 s[4:5], -1
	s_cbranch_scc0 .LBB0_223
	v_or_b32_e32 v4, s10, v2
	v_mov_b32_e32 v5, s11
	v_lshlrev_b64 v[4:5], 13, v[4:5]
	v_lshl_add_u64 v[4:5], s[38:39], 0, v[4:5]
	s_lshl_b32 s4, s13, 1
	s_mov_b32 s5, 0
	v_lshl_add_u64 v[4:5], v[4:5], 0, s[4:5]
	v_add_co_u32_e32 v4, vcc, 0x1000, v4
	s_lshl_b32 s1, s13, 2
	s_nop 0
	v_addc_co_u32_e32 v5, vcc, 0, v5, vcc
	global_load_ushort v3, v[4:5], off offset:3976
	v_mov_b32_e32 v6, s1
	global_load_dword v7, v6, s[62:63]
	s_nop 0
	global_load_dword v6, v6, s[60:61]
	s_nop 0
	global_load_ushort v4, v[4:5], off offset:3968
	s_mov_b32 s1, 0x41a00000
	v_mov_b32_e32 v8, 0
	v_mov_b32_e32 v9, 0
	v_mov_b32_e32 v5, 0
	v_mbcnt_lo_u32_b32 v10, -1, 0
	v_bfrev_b32_e32 v11, 0.5
	v_mbcnt_hi_u32_b32 v10, -1, v10
	v_lshl_or_b32 v10, v10, 2, v11
	s_waitcnt vmcnt(0)
	v_lshlrev_b32_e32 v3, 16, v3
	v_add_f32_e32 v3, v7, v3
	v_mul_f32_e32 v7, 0x3fb8aa3b, v3
	v_exp_f32_e32 v7, v7
	v_mul_f32_e32 v6, 0x3fb8aa3b, v6
	v_exp_f32_e32 v6, v6
	v_cmp_lt_f32_e32 vcc, s1, v3
	v_add_f32_e32 v7, 1.0, v7
	v_log_f32_e32 v7, v7
	v_lshlrev_b32_e32 v4, 16, v4
	v_mul_f32_e32 v4, 0xbfb8aa3b, v4
	v_exp_f32_e32 v4, v4
	v_mul_f32_e32 v7, 0x3f317218, v7
	v_cndmask_b32_e32 v3, v7, v3, vcc
	v_mul_f32_e64 v7, v3, -v6
	v_add_f32_e32 v4, 1.0, v4
	v_rcp_f32_e32 v4, v4
	v_mov_b32_dpp v8, v7 row_shr:1 row_mask:0xf bank_mask:0xf
	v_fma_f32 v3, v3, -v6, v8
	v_lshl_add_u32 v8, v2, 2, 0
	v_add_u32_e32 v8, 0x1b200, v8
	v_add_f32_dpp v3, v3, v3 row_shr:2 row_mask:0xf bank_mask:0xf bound_ctrl:1
	v_cmp_eq_u32_e32 vcc, 0, v2
	s_nop 0
	v_add_f32_dpp v3, v3, v3 row_shr:4 row_mask:0xf bank_mask:0xf bound_ctrl:1
	s_nop 1
	v_add_f32_dpp v3, v3, v3 row_shr:8 row_mask:0xf bank_mask:0xf bound_ctrl:1
	s_nop 1
	v_mov_b32_dpp v9, v3 row_bcast:15 row_mask:0xa bank_mask:0xf
	v_add_f32_e32 v3, v3, v9
	s_nop 1
	v_mov_b32_dpp v5, v3 row_bcast:31 row_mask:0xc bank_mask:0xf
	v_add_f32_e32 v5, v3, v5
	ds_bpermute_b32 v3, v10, v5
	v_mul_f32_e32 v6, 0x3fb8aa3b, v5
	v_exp_f32_e32 v6, v6
	s_waitcnt lgkmcnt(0)
	v_sub_f32_e32 v7, v3, v5
	v_mul_f32_e32 v7, 0x3fb8aa3b, v7
	v_exp_f32_e32 v7, v7
	ds_write2st64_b32 v8, v4, v5 offset1:1
	ds_write2st64_b32 v8, v6, v7 offset0:2 offset1:3
	s_and_saveexec_b64 s[4:5], vcc
	s_cbranch_execz .LBB0_222
	s_lshl_b32 s0, s0, 7
	s_lshl_b32 s1, s13, 5
	s_or_b32 s0, s0, s1
	s_add_i32 s0, s0, s12
	v_mul_f32_e32 v3, 0x3fb8aa3b, v3
	s_ashr_i32 s1, s0, 31
	v_exp_f32_e32 v3, v3
	s_lshl_b64 s[0:1], s[0:1], 2
	s_add_u32 s0, s50, s0
	s_addc_u32 s1, s51, s1
	v_mov_b32_e32 v4, 0xd90000
	global_store_dword v4, v3, s[0:1]

.LBB0_533:
	s_getpc_b64 s[98:99]
	s_and_b32 s98, s98, 0xffffff80
	v_readlane_b32 s97, v252, 2
	s_nop 0
	s_and_b32 s97, s97, 31
	s_mul_i32 s97, s97, 0x480
	s_add_u32 s98, s98, s97
	s_addc_u32 s99, s99, 0
	v_and_b32_e32 v254, 63, v0
	v_min_u32_e32 v254, 8, v254
	v_lshlrev_b32_e32 v254, 7, v254
	global_load_dword v254, v254, s[98:99]
	s_add_u32 s0, s50, 0xe00000
	s_addc_u32 s1, s51, 0
	s_add_u32 s56, s50, 0x1000000
	s_addc_u32 s57, s51, 0
	s_add_u32 s54, s50, 0xbc00000
	s_addc_u32 s55, s51, 0
	v_writelane_b32 v252, s0, 8
	s_cmp_lt_i32 s88, 4
	s_nop 0
	v_writelane_b32 v252, s1, 9
	s_cselect_b64 s[0:1], -1, 0
	s_cmp_gt_i32 s89, 3
	s_cselect_b64 s[4:5], -1, 0
	s_and_b64 s[0:1], s[0:1], s[4:5]
	s_andn2_b64 vcc, exec, s[0:1]
	s_cbranch_vccnz .LBB0_1294
	s_add_i32 s0, s84, -16
	v_readlane_b32 s1, v252, 2
	s_cmp_lt_i32 s1, s0
	s_cbranch_scc1 .LBB0_542
	v_lshlrev_b32_e32 v2, 4, v0
	v_and_b32_e32 v1, 32, v0
	v_bitop3_b32 v10, v2, v1, 48 bitop3:0x6c
	v_lshrrev_b32_e32 v1, 1, v0
	v_lshrrev_b32_e32 v4, 5, v0
	v_readlane_b32 s1, v252, 2
	v_and_b32_e32 v1, 24, v1
	v_and_b32_e32 v4, 4, v4
	v_bfe_u32 v5, v0, 2, 2
	s_sub_i32 s1, s1, s0
	v_readfirstlane_b32 s20, v0
	v_bfe_u32 v12, v0, 2, 4
	v_and_b32_e32 v11, 64, v0
	v_or3_b32 v4, v4, v5, v1
	v_lshrrev_b32_e32 v5, 3, v0
	v_or_b32_e32 v13, 0x2000, v2
	s_lshr_b32 s0, s1, 1
	s_and_b32 s21, s1, 1
	s_mov_b32 s1, 0
	v_or_b32_e32 v3, v10, v11
	v_and_or_b32 v6, v5, 48, v12
	v_and_or_b32 v5, v5, 32, v4
	v_lshrrev_b32_e32 v2, 7, v13
	s_movk_i32 s4, 0x70
	s_lshr_b32 s11, s20, 6
	s_lshr_b32 s10, s20, 8
	v_lshl_or_b32 v132, v5, 11, v3
	v_and_or_b32 v5, v2, s4, v12
	s_movk_i32 s4, 0x60
	s_lshl_b32 s16, s11, 10
	s_lshl_b64 s[12:13], s[0:1], 19
	s_lshl_b32 s14, s21, 19
	v_and_or_b32 v2, v2, s4, v4
	s_add_u32 s4, s8, s14
	s_addc_u32 s5, s9, 0
	s_add_i32 s1, s16, 0
	s_add_i32 m0, s1, 0x10000
	v_lshl_or_b32 v136, v2, 11, v3
	global_load_lds_dwordx4 v132, s[4:5]
	s_add_i32 m0, s1, 0x12000
	s_add_u32 s8, s4, 0x40000
	global_load_lds_dwordx4 v136, s[4:5]
	s_addc_u32 s9, s5, 0
	s_add_i32 m0, s1, 0x14000
	v_lshl_or_b32 v130, v6, 11, v3
	global_load_lds_dwordx4 v132, s[8:9]
	s_add_i32 m0, s1, 0x16000
	v_lshl_or_b32 v134, v5, 11, v3
	global_load_lds_dwordx4 v136, s[8:9]
	s_add_u32 s8, s69, s12
	s_addc_u32 s9, s70, s13
	s_add_i32 s22, s1, 0x2000
	s_mov_b32 m0, s1
	s_add_u32 s18, s8, 0x40000
	global_load_lds_dwordx4 v130, s[8:9]
	s_mov_b32 m0, s22
	s_addc_u32 s19, s9, 0
	s_add_i32 s23, s1, 0x4000
	global_load_lds_dwordx4 v134, s[8:9]
	s_mov_b32 m0, s23
	s_add_i32 s24, s1, 0x6000
	global_load_lds_dwordx4 v130, s[18:19]
	s_mov_b32 m0, s24
	v_mov_b32_e32 v133, 0
	global_load_lds_dwordx4 v134, s[18:19]
	v_mov_b32_e32 v137, v133
	v_mov_b32_e32 v131, v133
	v_mov_b32_e32 v135, v133
	v_lshl_add_u64 v[8:9], s[4:5], 0, v[132:133]
	v_lshl_add_u64 v[6:7], s[4:5], 0, v[136:137]
	v_lshl_add_u64 v[4:5], s[8:9], 0, v[130:131]
	s_cmp_lg_u32 s10, 1
	v_lshl_add_u64 v[2:3], s[8:9], 0, v[134:135]
	s_cbranch_scc1 .LBB0_537
	s_barrier

.LBB0_1294:
	s_getpc_b64 s[98:99]
	s_and_b32 s98, s98, 0xffffff80
	v_readlane_b32 s97, v252, 2
	s_nop 0
	s_and_b32 s97, s97, 31
	s_mul_i32 s97, s97, 0x300
	s_add_u32 s98, s98, s97
	s_addc_u32 s99, s99, 0
	v_and_b32_e32 v254, 63, v0
	v_min_u32_e32 v254, 5, v254
	v_lshlrev_b32_e32 v254, 7, v254
	global_load_dword v254, v254, s[98:99]
	s_cmp_lt_i32 s88, 5
	s_cselect_b64 s[0:1], -1, 0
	s_cmp_gt_i32 s89, 4
	s_cselect_b64 s[4:5], -1, 0
	s_and_b64 s[0:1], s[0:1], s[4:5]
	s_andn2_b64 vcc, exec, s[0:1]
	s_cbranch_vccnz .LBB0_1427
	s_cmp_lg_u32 s90, -1
	s_cselect_b64 s[0:1], -1, 0
	s_cmpk_lt_i32 s96, 0x4000
	s_cselect_b64 s[4:5], -1, 0
	s_and_b64 s[0:1], s[0:1], s[4:5]
	s_andn2_b64 vcc, exec, s[0:1]
	v_readlane_b32 s68, v252, 2
	s_cbranch_vccnz .LBB0_1314
	s_abs_i32 s3, s92
	v_cvt_f32_u32_e32 v1, s3
	s_sub_i32 s4, 0, s3
	v_readlane_b32 s1, v252, 6
	s_sub_i32 s1, s92, s1
	v_rcp_iflag_f32_e32 v1, v1
	s_ashr_i32 s93, s92, 31
	s_ashr_i32 s97, s96, 31
	s_lshl_b32 s0, s84, 5
	v_mul_f32_e32 v1, 0x4f7ffffe, v1
	v_cvt_u32_f32_e32 v1, v1
	s_lshl_b64 s[18:19], s[92:93], 12
	s_lshl_b64 s[20:21], s[96:97], 13
	s_mul_i32 s24, s92, 0x6000
	v_readfirstlane_b32 s5, v1
	s_mul_i32 s4, s4, s5
	s_mul_hi_u32 s4, s5, s4
	s_add_i32 s33, s5, s4
	v_readlane_b32 s4, v252, 7
	s_sub_i32 s1, s1, s4
	s_add_i32 s34, s1, 0x3fff
	s_add_u32 s1, s50, s20
	s_addc_u32 s5, s51, s21
	s_add_u32 s4, s1, 0x1800c00
	s_addc_u32 s5, s5, 0
	s_ashr_i32 s1, s0, 31
	s_lshl_b64 s[6:7], s[0:1], 13
	s_lshl_b64 s[22:23], s[96:97], 11
	s_add_u32 s8, s50, s22
	s_addc_u32 s9, s51, s23
	s_add_u32 s8, s8, 0xbc00000
	s_addc_u32 s9, s9, 0
	s_lshl_b64 s[10:11], s[0:1], 11
	s_add_u32 s14, s92, s96
	s_addc_u32 s15, s93, s97
	s_lshl_b64 s[12:13], s[14:15], 13
	s_add_u32 s1, s50, s12
	s_addc_u32 s13, s51, s13
	s_add_u32 s12, s1, 0x1800c00
	s_addc_u32 s13, s13, 0
	s_lshl_b64 s[14:15], s[14:15], 11
	s_add_u32 s1, s50, s14
	s_addc_u32 s15, s51, s15
	s_add_u32 s14, s1, 0xbc00000
	s_addc_u32 s15, s15, 0
	s_lshl_b64 s[16:17], s[92:93], 14
	s_add_u32 s1, s16, s20
	s_addc_u32 s16, s17, s21
	s_add_u32 s1, s50, s1
	s_addc_u32 s17, s51, s16
	s_add_u32 s16, s1, 0x1800c00
	s_addc_u32 s17, s17, 0
	s_add_u32 s1, s18, s22
	s_addc_u32 s18, s19, s23
	s_add_u32 s1, s50, s1
	s_addc_u32 s19, s51, s18
	s_add_u32 s18, s1, 0xbc00000
	s_addc_u32 s19, s19, 0
	s_mul_hi_i32 s1, s92, 0x6000
	s_add_u32 s20, s24, s20
	s_addc_u32 s1, s1, s21
	s_add_u32 s20, s50, s20
	s_addc_u32 s1, s51, s1
	s_add_u32 s20, s20, 0x1800c00
	s_addc_u32 s21, s1, 0
	s_mul_i32 s24, s92, 0x1800
	s_mul_hi_i32 s1, s92, 0x1800
	s_add_u32 s22, s24, s22
	s_addc_u32 s1, s1, s23
	s_add_u32 s22, s50, s22
	v_lshlrev_b32_e32 v2, 5, v198
	s_addc_u32 s1, s51, s1
	s_waitcnt vmcnt(0)
	v_mov_b32_e32 v43, 0
	v_and_b32_e32 v42, 0x1e0, v2
	s_add_u32 s22, s22, 0xbc00000
	v_mbcnt_lo_u32_b32 v2, -1, 0
	v_lshl_add_u64 v[44:45], s[64:65], 0, v[42:43]
	v_lshlrev_b32_e32 v42, 4, v198
	s_addc_u32 s23, s1, 0
	v_mov_b32_e32 v1, 0x358637bd
	v_mbcnt_hi_u32_b32 v48, -1, v2
	s_branch .LBB0_1298

.LBB0_1427:
	s_getpc_b64 s[98:99]
	s_and_b32 s98, s98, 0xffffff80
	v_readlane_b32 s97, v252, 2
	s_nop 0
	s_and_b32 s97, s97, 31
	s_mul_i32 s97, s97, 0x200
	s_add_u32 s98, s98, s97
	s_addc_u32 s99, s99, 0
	v_and_b32_e32 v254, 63, v0
	v_min_u32_e32 v254, 3, v254
	v_lshlrev_b32_e32 v254, 7, v254
	global_load_dword v254, v254, s[98:99]
	s_cmp_lt_i32 s88, 6
	s_cselect_b64 s[0:1], -1, 0
	s_cmp_gt_i32 s89, 5
	s_cselect_b64 s[4:5], -1, 0
	s_and_b64 s[0:1], s[0:1], s[4:5]
	s_andn2_b64 vcc, exec, s[0:1]
	s_cbranch_vccnz .LBB0_1492
	v_mov_b32_e32 v1, 0
	global_load_dword v206, v1, s[50:51] sc1
	v_mov_b32_e32 v1, 0x4000
	global_load_dword v207, v1, s[50:51] offset:512 sc1
	v_mov_b32_e32 v1, 0x7000
	global_load_dword v204, v1, s[50:51] offset:2048 sc1
	v_mov_b32_e32 v1, 0xa000
	global_load_dword v205, v1, s[50:51] offset:3584 sc1
	v_mov_b32_e32 v1, 0xe000
	global_load_dword v199, v1, s[50:51] offset:1024 sc1
	s_cmpk_gt_i32 s2, 0xff
	v_readfirstlane_b32 s28, v0
	s_cbranch_scc1 .LBB0_1492
	s_ashr_i32 s29, s2, 31
	s_lshr_b32 s0, s29, 29
	s_add_i32 s5, s2, s0
	s_and_b32 s0, s5, -8
	s_sub_i32 s3, s2, s0
	s_cmp_gt_i32 s3, -1
	s_cbranch_scc0 .LBB0_1431
	s_lshl_b32 s4, s3, 5
	s_mov_b64 s[0:1], 0
	s_branch .LBB0_1432
